# hybrid: QKV GEMM phases on 198/227 CUs (same rounds) with whole-phase converter CUs (11/19 items), WO/MoE2/attention tail conversion, + v75 micro edits; 4778 items hidden
# speedup vs baseline: 1.0031x; 1.0031x over previous
.LBB0_55:
	s_cmp_lg_u32 s99, 0
	s_cbranch_scc1 .Ltc_itemdone
	v_readlane_b32 s2, v254, 0
	v_readlane_b32 s3, v254, 1
	s_load_dword s0, s[2:3], 0xe8
	s_add_i32 s14, s14, s15
	s_add_i32 s16, s16, s17
	s_add_i32 s10, s10, s18
	s_waitcnt lgkmcnt(0)
	s_add_i32 s22, s22, s0
	s_cmp_lt_i32 s22, 0x1556
	s_cbranch_scc1 .Ltc_noskip
	s_cmp_ge_i32 s22, 0x2000
	s_cbranch_scc1 .Ltc_noskip
	s_and_b32 s22, s22, 0xff
	s_addk_i32 s22, 0x2000
	s_lshl_b32 s14, s22, 5
	s_lshl_b32 s16, s22, 4
	s_lshl_b32 s10, s22, 9

.Ltc_next:
	s_cmp_ge_u32 s100, 0x12aa
	s_cbranch_scc1 .Ltc_alldone
	s_movk_i32 s22, 0x1d56
	s_cmp_lt_u32 s100, 0xeaa
	s_cselect_b32 s22, 0x1156, s22
	s_cmp_lt_u32 s100, 0x6aa
	s_cselect_b32 s22, 0x2556, s22
	s_cmp_lt_u32 s100, 0x2aa
	s_cselect_b32 s22, 0x1556, s22
	s_add_i32 s22, s22, s100
	v_mbcnt_lo_u32_b32 v0, -1, 0
	v_mbcnt_hi_u32_b32 v0, -1, v0
	s_and_b32 s0, s94, 0xffffffc0
	s_nop 0
	v_ashrrev_i32_e32 v1, 31, v0
	v_add_u32_e32 v2, s0, v0
	s_movk_i32 s0, 0x44
	v_lshlrev_b32_e32 v5, 7, v0
	v_mul_lo_u32 v4, v0, s0
	v_mul_lo_u32 v12, v2, s0
	v_lshrrev_b32_e32 v3, 1, v2
	v_and_b32_e32 v5, 0x80, v5
	s_movk_i32 s0, 0x7f
	v_and_or_b32 v3, v3, s0, v5
	s_lshl_b32 s6, s95, 3
	s_add_u32 s7, s88, 0x22000000
	s_addc_u32 s11, s89, 0
	v_add_u32_e32 v4, 0, v4
	s_add_u32 s12, s88, 0x2000000
	v_add_u32_e32 v4, s6, v4
	s_mov_b32 s1, 0
	s_addc_u32 s13, s89, 0
	s_lshl_b32 s14, s22, 5
	s_lshl_b32 s16, s22, 4
	s_lshl_b32 s10, s22, 9
	s_mov_b32 s19, 0xc3e00000
	s_movk_i32 s20, 0xff
	v_add_u32_e32 v5, 0x1100, v4
	v_add_u32_e32 v6, 0x2200, v4
	v_add_u32_e32 v7, 0x3300, v4
	v_add_u32_e32 v8, 0x4400, v4
	v_add_u32_e32 v9, 0x5500, v4
	v_add_u32_e32 v10, 0x6600, v4
	v_add_u32_e32 v11, 0x7700, v4
	v_add_u32_e32 v12, 0, v12
	s_movk_i32 s21, 0xff00
	v_mov_b32_e32 v13, 0x43e00000
	v_mov_b32_e32 v14, 8
	s_branch .LBB0_56

.LBB0_187:
	v_readlane_b32 s14, v254, 0
	v_readlane_b32 s15, v254, 1
	s_movk_i32 s5, 0x100
	s_add_i32 s46, s46, 1
	s_waitcnt lgkmcnt(0)
	s_mul_i32 s5, s46, 0xc6
	s_add_i32 s5, s5, s96
	s_cmpk_lt_i32 s5, 0x318
	s_cselect_b64 s[16:17], -1, 0
	s_cmpk_gt_i32 s5, 0x317
	s_cbranch_scc1 .LBB0_189
	s_mul_hi_i32 s10, s5, 0x2aaaaaab
	s_lshr_b32 s11, s10, 31
	s_add_i32 s10, s10, s11
	s_mul_i32 s11, s10, -6
	s_add_i32 s12, s11, s5

.LBB0_359:
	s_cmp_lt_u32 s96, 32
	s_cbranch_scc1 .Ltc_skip_3
	v_writelane_b32 v200, s0, 0
	s_nop 1
	v_writelane_b32 v200, s1, 1
	s_nop 1
	v_writelane_b32 v200, s2, 2
	s_nop 1
	v_writelane_b32 v200, s3, 3
	s_nop 1
	v_writelane_b32 v200, s4, 4
	s_nop 1
	v_writelane_b32 v200, s5, 5
	s_nop 1
	v_writelane_b32 v200, s6, 6
	s_nop 1
	v_writelane_b32 v200, s7, 7
	s_nop 1
	v_writelane_b32 v200, s10, 8
	s_nop 1
	v_writelane_b32 v200, s11, 9
	s_nop 1
	v_writelane_b32 v200, s12, 10
	s_nop 1
	v_writelane_b32 v200, s13, 11
	s_nop 1
	v_writelane_b32 v200, s14, 12
	s_nop 1
	v_writelane_b32 v200, s15, 13
	s_nop 1
	v_writelane_b32 v200, s16, 14
	s_nop 1
	v_writelane_b32 v200, s17, 15
	s_nop 1
	v_writelane_b32 v200, s18, 16
	s_nop 1
	v_writelane_b32 v200, s19, 17
	s_nop 1
	v_writelane_b32 v200, s20, 18
	s_nop 1
	v_writelane_b32 v200, s21, 19
	s_nop 1
	v_writelane_b32 v200, s22, 20
	s_nop 1
	v_writelane_b32 v200, s23, 21
	s_nop 1
	v_writelane_b32 v200, s24, 22
	s_nop 1
	v_writelane_b32 v200, s25, 23
	s_nop 1
	v_writelane_b32 v200, s36, 24
	s_nop 1
	v_writelane_b32 v200, s37, 25
	s_nop 1
	v_writelane_b32 v200, s38, 26
	s_nop 1
	v_writelane_b32 v200, s39, 27
	s_nop 1
	v_writelane_b32 v200, s40, 28
	s_nop 1
	v_writelane_b32 v200, s41, 29
	s_nop 1
	v_writelane_b32 v200, s42, 30
	s_nop 1
	v_writelane_b32 v200, s43, 31
	s_nop 1
	v_writelane_b32 v200, s44, 32
	s_nop 1
	v_writelane_b32 v200, s45, 33
	s_nop 1
	v_writelane_b32 v200, s46, 34
	s_nop 1
	v_writelane_b32 v200, s47, 35
	s_nop 1
	v_writelane_b32 v200, s48, 36
	s_nop 1
	v_writelane_b32 v200, s49, 37
	s_nop 1
	v_writelane_b32 v200, s50, 38
	s_nop 1
	v_writelane_b32 v200, s51, 39
	s_nop 1
	s_mov_b32 s99, 3
	s_mov_b32 s98, 2
	s_mov_b32 s101, 224
	s_add_i32 s100, s96, 798
	s_branch .Ltc_next

.LBB0_668:
	s_cmp_lt_u32 s96, 144
	s_cbranch_scc1 .Ltc_skip_4
	v_writelane_b32 v200, s0, 0
	s_nop 1
	v_writelane_b32 v200, s1, 1
	s_nop 1
	v_writelane_b32 v200, s2, 2
	s_nop 1
	v_writelane_b32 v200, s3, 3
	s_nop 1
	v_writelane_b32 v200, s4, 4
	s_nop 1
	v_writelane_b32 v200, s5, 5
	s_nop 1
	v_writelane_b32 v200, s6, 6
	s_nop 1
	v_writelane_b32 v200, s7, 7
	s_nop 1
	v_writelane_b32 v200, s10, 8
	s_nop 1
	v_writelane_b32 v200, s11, 9
	s_nop 1
	v_writelane_b32 v200, s12, 10
	s_nop 1
	v_writelane_b32 v200, s13, 11
	s_nop 1
	v_writelane_b32 v200, s14, 12
	s_nop 1
	v_writelane_b32 v200, s15, 13
	s_nop 1
	v_writelane_b32 v200, s16, 14
	s_nop 1
	v_writelane_b32 v200, s17, 15
	s_nop 1
	v_writelane_b32 v200, s18, 16
	s_nop 1
	v_writelane_b32 v200, s19, 17
	s_nop 1
	v_writelane_b32 v200, s20, 18
	s_nop 1
	v_writelane_b32 v200, s21, 19
	s_nop 1
	v_writelane_b32 v200, s22, 20
	s_nop 1
	v_writelane_b32 v200, s23, 21
	s_nop 1
	v_writelane_b32 v200, s24, 22
	s_nop 1
	v_writelane_b32 v200, s25, 23
	s_nop 1
	v_writelane_b32 v200, s36, 24
	s_nop 1
	v_writelane_b32 v200, s37, 25
	s_nop 1
	v_writelane_b32 v200, s38, 26
	s_nop 1
	v_writelane_b32 v200, s39, 27
	s_nop 1
	v_writelane_b32 v200, s40, 28
	s_nop 1
	v_writelane_b32 v200, s41, 29
	s_nop 1
	v_writelane_b32 v200, s42, 30
	s_nop 1
	v_writelane_b32 v200, s43, 31
	s_nop 1
	v_writelane_b32 v200, s44, 32
	s_nop 1
	v_writelane_b32 v200, s45, 33
	s_nop 1
	v_writelane_b32 v200, s46, 34
	s_nop 1
	v_writelane_b32 v200, s47, 35
	s_nop 1
	v_writelane_b32 v200, s48, 36
	s_nop 1
	v_writelane_b32 v200, s49, 37
	s_nop 1
	v_writelane_b32 v200, s50, 38
	s_nop 1
	v_writelane_b32 v200, s51, 39
	s_nop 1
	s_mov_b32 s99, 4
	s_mov_b32 s98, 2
	s_mov_b32 s101, 112
	s_add_i32 s100, s96, 1134
	s_branch .Ltc_next

.LBB0_797:
	v_readlane_b32 s10, v254, 0
	v_readlane_b32 s11, v254, 1
	s_movk_i32 s7, 0x100
	s_add_i32 s43, s43, 1
	s_waitcnt lgkmcnt(0)
	s_mul_i32 s7, s43, 0xe3
	s_add_i32 s7, s7, s96
	s_cmpk_lt_i32 s7, 0x630
	s_cselect_b64 s[12:13], -1, 0
	s_cmpk_gt_i32 s7, 0x62f
	s_cbranch_scc1 .LBB0_799
	s_mul_hi_i32 s6, s7, 0x2aaaaaab
	s_lshr_b32 s8, s6, 31
	s_ashr_i32 s6, s6, 1
	s_add_i32 s6, s6, s8
	s_mul_i32 s8, s6, -12
	s_add_i32 s8, s8, s7

.LBB0_807:
	s_cmp_lt_u32 s96, 227
	s_cbranch_scc1 .Ltc_skip_5
	v_writelane_b32 v200, s0, 0
	s_nop 1
	v_writelane_b32 v200, s1, 1
	s_nop 1
	v_writelane_b32 v200, s2, 2
	s_nop 1
	v_writelane_b32 v200, s3, 3
	s_nop 1
	v_writelane_b32 v200, s4, 4
	s_nop 1
	v_writelane_b32 v200, s5, 5
	s_nop 1
	v_writelane_b32 v200, s6, 6
	s_nop 1
	v_writelane_b32 v200, s7, 7
	s_nop 1
	v_writelane_b32 v200, s10, 8
	s_nop 1
	v_writelane_b32 v200, s11, 9
	s_nop 1
	v_writelane_b32 v200, s12, 10
	s_nop 1
	v_writelane_b32 v200, s13, 11
	s_nop 1
	v_writelane_b32 v200, s14, 12
	s_nop 1
	v_writelane_b32 v200, s15, 13
	s_nop 1
	v_writelane_b32 v200, s16, 14
	s_nop 1
	v_writelane_b32 v200, s17, 15
	s_nop 1
	v_writelane_b32 v200, s18, 16
	s_nop 1
	v_writelane_b32 v200, s19, 17
	s_nop 1
	v_writelane_b32 v200, s20, 18
	s_nop 1
	v_writelane_b32 v200, s21, 19
	s_nop 1
	v_writelane_b32 v200, s22, 20
	s_nop 1
	v_writelane_b32 v200, s23, 21
	s_nop 1
	v_writelane_b32 v200, s24, 22
	s_nop 1
	v_writelane_b32 v200, s25, 23
	s_nop 1
	v_writelane_b32 v200, s36, 24
	s_nop 1
	v_writelane_b32 v200, s37, 25
	s_nop 1
	v_writelane_b32 v200, s38, 26
	s_nop 1
	v_writelane_b32 v200, s39, 27
	s_nop 1
	v_writelane_b32 v200, s40, 28
	s_nop 1
	v_writelane_b32 v200, s41, 29
	s_nop 1
	v_writelane_b32 v200, s42, 30
	s_nop 1
	v_writelane_b32 v200, s43, 31
	s_nop 1
	v_writelane_b32 v200, s44, 32
	s_nop 1
	v_writelane_b32 v200, s45, 33
	s_nop 1
	v_writelane_b32 v200, s46, 34
	s_nop 1
	v_writelane_b32 v200, s47, 35
	s_nop 1
	v_writelane_b32 v200, s48, 36
	s_nop 1
	v_writelane_b32 v200, s49, 37
	s_nop 1
	v_writelane_b32 v200, s50, 38
	s_nop 1
	v_writelane_b32 v200, s51, 39
	s_nop 1
	s_mov_b32 s99, 5
	s_mov_b32 s98, 19
	s_mov_b32 s101, 29
	s_add_i32 s100, s96, 1275
	s_branch .Ltc_next

.LBB0_1052:
	s_cmp_lt_u32 s96, 32
	s_cbranch_scc1 .Ltc_skip_6
	v_writelane_b32 v200, s0, 0
	s_nop 1
	v_writelane_b32 v200, s1, 1
	s_nop 1
	v_writelane_b32 v200, s2, 2
	s_nop 1
	v_writelane_b32 v200, s3, 3
	s_nop 1
	v_writelane_b32 v200, s4, 4
	s_nop 1
	v_writelane_b32 v200, s5, 5
	s_nop 1
	v_writelane_b32 v200, s6, 6
	s_nop 1
	v_writelane_b32 v200, s7, 7
	s_nop 1
	v_writelane_b32 v200, s10, 8
	s_nop 1
	v_writelane_b32 v200, s11, 9
	s_nop 1
	v_writelane_b32 v200, s12, 10
	s_nop 1
	v_writelane_b32 v200, s13, 11
	s_nop 1
	v_writelane_b32 v200, s14, 12
	s_nop 1
	v_writelane_b32 v200, s15, 13
	s_nop 1
	v_writelane_b32 v200, s16, 14
	s_nop 1
	v_writelane_b32 v200, s17, 15
	s_nop 1
	v_writelane_b32 v200, s18, 16
	s_nop 1
	v_writelane_b32 v200, s19, 17
	s_nop 1
	v_writelane_b32 v200, s20, 18
	s_nop 1
	v_writelane_b32 v200, s21, 19
	s_nop 1
	v_writelane_b32 v200, s22, 20
	s_nop 1
	v_writelane_b32 v200, s23, 21
	s_nop 1
	v_writelane_b32 v200, s24, 22
	s_nop 1
	v_writelane_b32 v200, s25, 23
	s_nop 1
	v_writelane_b32 v200, s36, 24
	s_nop 1
	v_writelane_b32 v200, s37, 25
	s_nop 1
	v_writelane_b32 v200, s38, 26
	s_nop 1
	v_writelane_b32 v200, s39, 27
	s_nop 1
	v_writelane_b32 v200, s40, 28
	s_nop 1
	v_writelane_b32 v200, s41, 29
	s_nop 1
	v_writelane_b32 v200, s42, 30
	s_nop 1
	v_writelane_b32 v200, s43, 31
	s_nop 1
	v_writelane_b32 v200, s44, 32
	s_nop 1
	v_writelane_b32 v200, s45, 33
	s_nop 1
	v_writelane_b32 v200, s46, 34
	s_nop 1
	v_writelane_b32 v200, s47, 35
	s_nop 1
	v_writelane_b32 v200, s48, 36
	s_nop 1
	v_writelane_b32 v200, s49, 37
	s_nop 1
	v_writelane_b32 v200, s50, 38
	s_nop 1
	v_writelane_b32 v200, s51, 39
	s_nop 1
	s_mov_b32 s99, 6
	s_mov_b32 s98, 2
	s_mov_b32 s101, 224
	s_add_i32 s100, s96, 2021
	s_branch .Ltc_next

.LBB0_1361:
	s_cmp_lt_u32 s96, 144
	s_cbranch_scc1 .Ltc_skip_7
	v_writelane_b32 v200, s0, 0
	s_nop 1
	v_writelane_b32 v200, s1, 1
	s_nop 1
	v_writelane_b32 v200, s2, 2
	s_nop 1
	v_writelane_b32 v200, s3, 3
	s_nop 1
	v_writelane_b32 v200, s4, 4
	s_nop 1
	v_writelane_b32 v200, s5, 5
	s_nop 1
	v_writelane_b32 v200, s6, 6
	s_nop 1
	v_writelane_b32 v200, s7, 7
	s_nop 1
	v_writelane_b32 v200, s10, 8
	s_nop 1
	v_writelane_b32 v200, s11, 9
	s_nop 1
	v_writelane_b32 v200, s12, 10
	s_nop 1
	v_writelane_b32 v200, s13, 11
	s_nop 1
	v_writelane_b32 v200, s14, 12
	s_nop 1
	v_writelane_b32 v200, s15, 13
	s_nop 1
	v_writelane_b32 v200, s16, 14
	s_nop 1
	v_writelane_b32 v200, s17, 15
	s_nop 1
	v_writelane_b32 v200, s18, 16
	s_nop 1
	v_writelane_b32 v200, s19, 17
	s_nop 1
	v_writelane_b32 v200, s20, 18
	s_nop 1
	v_writelane_b32 v200, s21, 19
	s_nop 1
	v_writelane_b32 v200, s22, 20
	s_nop 1
	v_writelane_b32 v200, s23, 21
	s_nop 1
	v_writelane_b32 v200, s24, 22
	s_nop 1
	v_writelane_b32 v200, s25, 23
	s_nop 1
	v_writelane_b32 v200, s36, 24
	s_nop 1
	v_writelane_b32 v200, s37, 25
	s_nop 1
	v_writelane_b32 v200, s38, 26
	s_nop 1
	v_writelane_b32 v200, s39, 27
	s_nop 1
	v_writelane_b32 v200, s40, 28
	s_nop 1
	v_writelane_b32 v200, s41, 29
	s_nop 1
	v_writelane_b32 v200, s42, 30
	s_nop 1
	v_writelane_b32 v200, s43, 31
	s_nop 1
	v_writelane_b32 v200, s44, 32
	s_nop 1
	v_writelane_b32 v200, s45, 33
	s_nop 1
	v_writelane_b32 v200, s46, 34
	s_nop 1
	v_writelane_b32 v200, s47, 35
	s_nop 1
	v_writelane_b32 v200, s48, 36
	s_nop 1
	v_writelane_b32 v200, s49, 37
	s_nop 1
	v_writelane_b32 v200, s50, 38
	s_nop 1
	v_writelane_b32 v200, s51, 39
	s_nop 1
	s_mov_b32 s99, 7
	s_mov_b32 s98, 2
	s_mov_b32 s101, 112
	s_add_i32 s100, s96, 2357
	s_branch .Ltc_s1_back

.LBB0_1495:
	s_cmp_lt_u32 s96, 227
	s_cbranch_scc1 .Ltc_skip_8
	v_writelane_b32 v200, s0, 0
	s_nop 1
	v_writelane_b32 v200, s1, 1
	s_nop 1
	v_writelane_b32 v200, s2, 2
	s_nop 1
	v_writelane_b32 v200, s3, 3
	s_nop 1
	v_writelane_b32 v200, s4, 4
	s_nop 1
	v_writelane_b32 v200, s5, 5
	s_nop 1
	v_writelane_b32 v200, s6, 6
	s_nop 1
	v_writelane_b32 v200, s7, 7
	s_nop 1
	v_writelane_b32 v200, s10, 8
	s_nop 1
	v_writelane_b32 v200, s11, 9
	s_nop 1
	v_writelane_b32 v200, s12, 10
	s_nop 1
	v_writelane_b32 v200, s13, 11
	s_nop 1
	v_writelane_b32 v200, s14, 12
	s_nop 1
	v_writelane_b32 v200, s15, 13
	s_nop 1
	v_writelane_b32 v200, s16, 14
	s_nop 1
	v_writelane_b32 v200, s17, 15
	s_nop 1
	v_writelane_b32 v200, s18, 16
	s_nop 1
	v_writelane_b32 v200, s19, 17
	s_nop 1
	v_writelane_b32 v200, s20, 18
	s_nop 1
	v_writelane_b32 v200, s21, 19
	s_nop 1
	v_writelane_b32 v200, s22, 20
	s_nop 1
	v_writelane_b32 v200, s23, 21
	s_nop 1
	v_writelane_b32 v200, s24, 22
	s_nop 1
	v_writelane_b32 v200, s25, 23
	s_nop 1
	v_writelane_b32 v200, s36, 24
	s_nop 1
	v_writelane_b32 v200, s37, 25
	s_nop 1
	v_writelane_b32 v200, s38, 26
	s_nop 1
	v_writelane_b32 v200, s39, 27
	s_nop 1
	v_writelane_b32 v200, s40, 28
	s_nop 1
	v_writelane_b32 v200, s41, 29
	s_nop 1
	v_writelane_b32 v200, s42, 30
	s_nop 1
	v_writelane_b32 v200, s43, 31
	s_nop 1
	v_writelane_b32 v200, s44, 32
	s_nop 1
	v_writelane_b32 v200, s45, 33
	s_nop 1
	v_writelane_b32 v200, s46, 34
	s_nop 1
	v_writelane_b32 v200, s47, 35
	s_nop 1
	v_writelane_b32 v200, s48, 36
	s_nop 1
	v_writelane_b32 v200, s49, 37
	s_nop 1
	v_writelane_b32 v200, s50, 38
	s_nop 1
	v_writelane_b32 v200, s51, 39
	s_nop 1
	s_mov_b32 s99, 8
	s_mov_b32 s98, 19
	s_mov_b32 s101, 29
	s_add_i32 s100, s96, 2498
	s_branch .Ltc_s1_back

.LBB0_1636:
	s_cmp_lt_u32 s96, 64
	s_cbranch_scc1 .Ltc_skip_9
	v_writelane_b32 v200, s0, 0
	s_nop 1
	v_writelane_b32 v200, s1, 1
	s_nop 1
	v_writelane_b32 v200, s2, 2
	s_nop 1
	v_writelane_b32 v200, s3, 3
	s_nop 1
	v_writelane_b32 v200, s4, 4
	s_nop 1
	v_writelane_b32 v200, s5, 5
	s_nop 1
	v_writelane_b32 v200, s6, 6
	s_nop 1
	v_writelane_b32 v200, s7, 7
	s_nop 1
	v_writelane_b32 v200, s10, 8
	s_nop 1
	v_writelane_b32 v200, s11, 9
	s_nop 1
	v_writelane_b32 v200, s12, 10
	s_nop 1
	v_writelane_b32 v200, s13, 11
	s_nop 1
	v_writelane_b32 v200, s14, 12
	s_nop 1
	v_writelane_b32 v200, s15, 13
	s_nop 1
	v_writelane_b32 v200, s16, 14
	s_nop 1
	v_writelane_b32 v200, s17, 15
	s_nop 1
	v_writelane_b32 v200, s18, 16
	s_nop 1
	v_writelane_b32 v200, s19, 17
	s_nop 1
	v_writelane_b32 v200, s20, 18
	s_nop 1
	v_writelane_b32 v200, s21, 19
	s_nop 1
	v_writelane_b32 v200, s22, 20
	s_nop 1
	v_writelane_b32 v200, s23, 21
	s_nop 1
	v_writelane_b32 v200, s24, 22
	s_nop 1
	v_writelane_b32 v200, s25, 23
	s_nop 1
	v_writelane_b32 v200, s36, 24
	s_nop 1
	v_writelane_b32 v200, s37, 25
	s_nop 1
	v_writelane_b32 v200, s38, 26
	s_nop 1
	v_writelane_b32 v200, s39, 27
	s_nop 1
	v_writelane_b32 v200, s40, 28
	s_nop 1
	v_writelane_b32 v200, s41, 29
	s_nop 1
	v_writelane_b32 v200, s42, 30
	s_nop 1
	v_writelane_b32 v200, s43, 31
	s_nop 1
	v_writelane_b32 v200, s44, 32
	s_nop 1
	v_writelane_b32 v200, s45, 33
	s_nop 1
	v_writelane_b32 v200, s46, 34
	s_nop 1
	v_writelane_b32 v200, s47, 35
	s_nop 1
	v_writelane_b32 v200, s48, 36
	s_nop 1
	v_writelane_b32 v200, s49, 37
	s_nop 1
	v_writelane_b32 v200, s50, 38
	s_nop 1
	v_writelane_b32 v200, s51, 39
	s_nop 1
	s_mov_b32 s99, 9
	s_mov_b32 s98, 1
	s_mov_b32 s101, 192
	s_add_i32 s100, s96, 3212
	s_branch .Ltc_s1_back

.LBB0_1711:
	s_cmp_lt_u32 s96, 32
	s_cbranch_scc1 .Ltc_skip_10
	v_writelane_b32 v200, s0, 0
	s_nop 1
	v_writelane_b32 v200, s1, 1
	s_nop 1
	v_writelane_b32 v200, s2, 2
	s_nop 1
	v_writelane_b32 v200, s3, 3
	s_nop 1
	v_writelane_b32 v200, s4, 4
	s_nop 1
	v_writelane_b32 v200, s5, 5
	s_nop 1
	v_writelane_b32 v200, s6, 6
	s_nop 1
	v_writelane_b32 v200, s7, 7
	s_nop 1
	v_writelane_b32 v200, s10, 8
	s_nop 1
	v_writelane_b32 v200, s11, 9
	s_nop 1
	v_writelane_b32 v200, s12, 10
	s_nop 1
	v_writelane_b32 v200, s13, 11
	s_nop 1
	v_writelane_b32 v200, s14, 12
	s_nop 1
	v_writelane_b32 v200, s15, 13
	s_nop 1
	v_writelane_b32 v200, s16, 14
	s_nop 1
	v_writelane_b32 v200, s17, 15
	s_nop 1
	v_writelane_b32 v200, s18, 16
	s_nop 1
	v_writelane_b32 v200, s19, 17
	s_nop 1
	v_writelane_b32 v200, s20, 18
	s_nop 1
	v_writelane_b32 v200, s21, 19
	s_nop 1
	v_writelane_b32 v200, s22, 20
	s_nop 1
	v_writelane_b32 v200, s23, 21
	s_nop 1
	v_writelane_b32 v200, s24, 22
	s_nop 1
	v_writelane_b32 v200, s25, 23
	s_nop 1
	v_writelane_b32 v200, s36, 24
	s_nop 1
	v_writelane_b32 v200, s37, 25
	s_nop 1
	v_writelane_b32 v200, s38, 26
	s_nop 1
	v_writelane_b32 v200, s39, 27
	s_nop 1
	v_writelane_b32 v200, s40, 28
	s_nop 1
	v_writelane_b32 v200, s41, 29
	s_nop 1
	v_writelane_b32 v200, s42, 30
	s_nop 1
	v_writelane_b32 v200, s43, 31
	s_nop 1
	v_writelane_b32 v200, s44, 32
	s_nop 1
	v_writelane_b32 v200, s45, 33
	s_nop 1
	v_writelane_b32 v200, s46, 34
	s_nop 1
	v_writelane_b32 v200, s47, 35
	s_nop 1
	v_writelane_b32 v200, s48, 36
	s_nop 1
	v_writelane_b32 v200, s49, 37
	s_nop 1
	v_writelane_b32 v200, s50, 38
	s_nop 1
	v_writelane_b32 v200, s51, 39
	s_nop 1
	s_mov_b32 s99, 10
	s_mov_b32 s98, 2
	s_mov_b32 s101, 224
	s_add_i32 s100, s96, 3436
	s_branch .Ltc_s1_back

.LBB0_2020:
	s_cmp_lt_u32 s96, 144
	s_cbranch_scc1 .Ltc_skip_11
	v_writelane_b32 v200, s0, 0
	s_nop 1
	v_writelane_b32 v200, s1, 1
	s_nop 1
	v_writelane_b32 v200, s2, 2
	s_nop 1
	v_writelane_b32 v200, s3, 3
	s_nop 1
	v_writelane_b32 v200, s4, 4
	s_nop 1
	v_writelane_b32 v200, s5, 5
	s_nop 1
	v_writelane_b32 v200, s6, 6
	s_nop 1
	v_writelane_b32 v200, s7, 7
	s_nop 1
	v_writelane_b32 v200, s10, 8
	s_nop 1
	v_writelane_b32 v200, s11, 9
	s_nop 1
	v_writelane_b32 v200, s12, 10
	s_nop 1
	v_writelane_b32 v200, s13, 11
	s_nop 1
	v_writelane_b32 v200, s14, 12
	s_nop 1
	v_writelane_b32 v200, s15, 13
	s_nop 1
	v_writelane_b32 v200, s16, 14
	s_nop 1
	v_writelane_b32 v200, s17, 15
	s_nop 1
	v_writelane_b32 v200, s18, 16
	s_nop 1
	v_writelane_b32 v200, s19, 17
	s_nop 1
	v_writelane_b32 v200, s20, 18
	s_nop 1
	v_writelane_b32 v200, s21, 19
	s_nop 1
	v_writelane_b32 v200, s22, 20
	s_nop 1
	v_writelane_b32 v200, s23, 21
	s_nop 1
	v_writelane_b32 v200, s24, 22
	s_nop 1
	v_writelane_b32 v200, s25, 23
	s_nop 1
	v_writelane_b32 v200, s36, 24
	s_nop 1
	v_writelane_b32 v200, s37, 25
	s_nop 1
	v_writelane_b32 v200, s38, 26
	s_nop 1
	v_writelane_b32 v200, s39, 27
	s_nop 1
	v_writelane_b32 v200, s40, 28
	s_nop 1
	v_writelane_b32 v200, s41, 29
	s_nop 1
	v_writelane_b32 v200, s42, 30
	s_nop 1
	v_writelane_b32 v200, s43, 31
	s_nop 1
	v_writelane_b32 v200, s44, 32
	s_nop 1
	v_writelane_b32 v200, s45, 33
	s_nop 1
	v_writelane_b32 v200, s46, 34
	s_nop 1
	v_writelane_b32 v200, s47, 35
	s_nop 1
	v_writelane_b32 v200, s48, 36
	s_nop 1
	v_writelane_b32 v200, s49, 37
	s_nop 1
	v_writelane_b32 v200, s50, 38
	s_nop 1
	v_writelane_b32 v200, s51, 39
	s_nop 1
	s_mov_b32 s99, 11
	s_mov_b32 s98, 2
	s_mov_b32 s101, 112
	s_add_i32 s100, s96, 3772
	s_branch .Ltc_s2_back

.LBB0_2154:
	s_cmp_lt_u32 s96, 198
	s_cbranch_scc1 .Ltc_skip_12
	v_writelane_b32 v200, s0, 0
	s_nop 1
	v_writelane_b32 v200, s1, 1
	s_nop 1
	v_writelane_b32 v200, s2, 2
	s_nop 1
	v_writelane_b32 v200, s3, 3
	s_nop 1
	v_writelane_b32 v200, s4, 4
	s_nop 1
	v_writelane_b32 v200, s5, 5
	s_nop 1
	v_writelane_b32 v200, s6, 6
	s_nop 1
	v_writelane_b32 v200, s7, 7
	s_nop 1
	v_writelane_b32 v200, s10, 8
	s_nop 1
	v_writelane_b32 v200, s11, 9
	s_nop 1
	v_writelane_b32 v200, s12, 10
	s_nop 1
	v_writelane_b32 v200, s13, 11
	s_nop 1
	v_writelane_b32 v200, s14, 12
	s_nop 1
	v_writelane_b32 v200, s15, 13
	s_nop 1
	v_writelane_b32 v200, s16, 14
	s_nop 1
	v_writelane_b32 v200, s17, 15
	s_nop 1
	v_writelane_b32 v200, s18, 16
	s_nop 1
	v_writelane_b32 v200, s19, 17
	s_nop 1
	v_writelane_b32 v200, s20, 18
	s_nop 1
	v_writelane_b32 v200, s21, 19
	s_nop 1
	v_writelane_b32 v200, s22, 20
	s_nop 1
	v_writelane_b32 v200, s23, 21
	s_nop 1
	v_writelane_b32 v200, s24, 22
	s_nop 1
	v_writelane_b32 v200, s25, 23
	s_nop 1
	v_writelane_b32 v200, s36, 24
	s_nop 1
	v_writelane_b32 v200, s37, 25
	s_nop 1
	v_writelane_b32 v200, s38, 26
	s_nop 1
	v_writelane_b32 v200, s39, 27
	s_nop 1
	v_writelane_b32 v200, s40, 28
	s_nop 1
	v_writelane_b32 v200, s41, 29
	s_nop 1
	v_writelane_b32 v200, s42, 30
	s_nop 1
	v_writelane_b32 v200, s43, 31
	s_nop 1
	v_writelane_b32 v200, s44, 32
	s_nop 1
	v_writelane_b32 v200, s45, 33
	s_nop 1
	v_writelane_b32 v200, s46, 34
	s_nop 1
	v_writelane_b32 v200, s47, 35
	s_nop 1
	v_writelane_b32 v200, s48, 36
	s_nop 1
	v_writelane_b32 v200, s49, 37
	s_nop 1
	v_writelane_b32 v200, s50, 38
	s_nop 1
	v_writelane_b32 v200, s51, 39
	s_nop 1
	s_mov_b32 s99, 12
	s_mov_b32 s98, 11
	s_mov_b32 s101, 58
	s_add_i32 s100, s96, 3942
	s_branch .Ltc_s2_back
